# P7: W_down slab split index regrouped so that each XCD's CUs pause together in two groups of 16 (upos = 2*xcd + half) to keep tile sharers in step for L2 reuse
# speedup vs baseline: 1.0132x; 1.0132x over previous
; __device__ __forceinline__ void do_slabs(Frame& F, int j0, int j1) { do_slabs_impl(F.lds, F.ws, F.w_up, F.w_dn, F.w_in, F.vcu, F.G, F.wave, j0, j1); }
; __global__ void __launch_bounds__(NTHR, 2) fwd(Args args) {
;     ...
;     if (IN(7) || IN(8) || IN(9)) build_tstart(F, tstart);
;     if (IN(7)) { FRAME_RELOAD();
;         build_units(F, tstart, 16, bc);
;         const int upos = (int)((blockIdx.x >> 3) & 15);
; #pragma unroll 1
;         for (int part = 0; part < 2; ++part) {
;             if (part == 1) do_slabs(F, 0, nDn);
;             SchedMoEUpT S; S.nt = D / 128; S.pitchA = D / 2; S.pitchB = D / 2; S.multA = 1; S.multB = 1; S.G = F.G; S.c = bc; S.wv = F.wave; S.A = (const char*)WSP(char, WS_H1Q); S.Bt = (const char*)WSP(char, WS_WUP);
;             S.tstart = tstart; S.row_tok = WSP(int, WS_RT) + 12 * T; S.cnt = F.ctl + CW_CNT; S.nN = 16; S.rowbytes = D; S.estride = (size_t)2 * DFF * D;
;             S.rsc = WSP(float, WS_RSC); S.swup = WSP(float, WS_SWUP); S.b_up = F.b_up;
;             S.u0 = part ? upos : 0; S.u1 = part ? 64 : upos;
;             EpiUp E{(unsigned char*)(F.ws + WS_ACTQ)};
;             gm::gemm_run<EpiUp, SchedMoEUpT, true, true, true>(F.lds, S, E);
.LBB0_1577:
	v_writelane_b32 v255, s10, 25
	s_nop 1
	v_writelane_b32 v255, s11, 26
	s_or_b64 exec, exec, s[6:7]
	s_and_b32 s24, s86, 7
	s_lshl_b32 s24, s24, 1
	s_bfe_u32 s98, s86, 0x10007
	s_or_b32 s24, s24, s98
	s_mov_b32 s0, s86
	s_cmp_gt_i32 s79, 0
	v_writelane_b32 v255, s0, 27
	s_cselect_b64 s[26:27], -1, 0
	s_cmpk_gt_i32 s78, 0x7ff
	v_writelane_b32 v255, s1, 28
	s_cselect_b64 s[0:1], -1, 0
	v_writelane_b32 v255, s0, 34
	s_cmpk_lt_i32 s78, 0x800
	s_mov_b32 s17, 0
	v_writelane_b32 v255, s1, 35
	s_cselect_b64 s[0:1], -1, 0
	s_lshl_b32 s2, s78, 5
	s_ashr_i32 s6, s78, 6
	s_and_b32 s2, s2, 0x7e0
	s_waitcnt lgkmcnt(0)
	s_add_u32 s8, s4, 0x21e00000
	s_addc_u32 s9, s5, 0
	v_writelane_b32 v255, s8, 39
	v_cndmask_b32_e64 v0, 0, 1, s[0:1]
	s_add_u32 s25, s4, 0x35e80000
	v_writelane_b32 v255, s9, 40
	v_readfirstlane_b32 s0, v0
	s_addc_u32 s30, s5, 0
	s_ashr_i32 s7, s6, 31
	v_writelane_b32 v255, s0, 43
	s_mov_b32 s0, s6
	v_writelane_b32 v255, s0, 36
	v_mbcnt_lo_u32_b32 v0, -1, 0
	s_mov_b64 s[34:35], -1
	v_writelane_b32 v255, s1, 37
	s_lshl_b64 s[0:1], s[6:7], 24
	s_add_u32 s0, s14, s0
	s_addc_u32 s1, s15, s1
	v_writelane_b32 v255, s2, 38
	s_lshl_b32 s2, s2, 2
	s_add_u32 s0, s0, s2
	s_addc_u32 s1, s1, 0
	v_writelane_b32 v255, s0, 49
	s_mov_b64 s[6:7], 0
	v_mov_b32_e32 v193, 0
	v_writelane_b32 v255, s1, 50
	s_lshl_b32 s0, s85, 7
	s_add_i32 s0, s0, 0
	s_add_i32 s0, s0, 0x20200
	s_add_u32 s38, s4, 0x69f00000
	s_addc_u32 s39, s5, 0
	v_writelane_b32 v255, s0, 44
	s_add_u32 s0, s4, 0x1e00000
	v_writelane_b32 v255, s0, 20
	s_addc_u32 s0, s5, 0
	v_writelane_b32 v255, s0, 24
	s_add_u32 s0, s4, 0x6dfc0000
	v_writelane_b32 v255, s0, 14
	s_addc_u32 s0, s5, 0
	v_writelane_b32 v255, s0, 16
	s_add_u32 s0, s4, 0x8000
	s_addc_u32 s47, s5, 0
	s_add_u32 s84, s4, 0x6c700000
	s_addc_u32 s86, s5, 0
	v_writelane_b32 v255, s0, 18
	s_add_u32 s0, s4, 0x180000
	v_writelane_b32 v255, s0, 19
	s_addc_u32 s0, s5, 0
	v_writelane_b32 v255, s0, 22
	s_add_u32 s91, s4, 0x92300000
	v_readlane_b32 s2, v255, 12
	s_addc_u32 s92, s5, 0
	s_lshr_b32 s0, s2, 8
	s_lshl_b32 s1, s0, 13
	v_writelane_b32 v255, s1, 45
	s_lshl_b32 s1, s85, 5
	s_and_b32 s96, s1, 0x60
	s_lshl_b32 s93, s85, 10
	s_lshl_b32 s94, s0, 6
	s_lshr_b32 s1, s96, 3
	s_and_b32 s10, s2, 0xc0
	s_cmpk_lt_u32 s2, 0x100
	s_cselect_b64 s[4:5], -1, 0
	s_cmp_eq_u32 s0, 1
	v_writelane_b32 v255, s1, 46
	s_cselect_b64 s[0:1], -1, 0
	v_writelane_b32 v255, s0, 47
	s_and_b32 s11, s2, 0xffffff00
	s_max_i32 s28, s79, 1
	v_writelane_b32 v255, s1, 48
	v_writelane_b32 v255, s24, 31
	v_writelane_b32 v255, s26, 32
	s_movk_i32 s29, 0x1010
	s_mov_b32 s23, 0x1fffe0
	v_writelane_b32 v255, s27, 33
	v_writelane_b32 v255, s25, 41
	s_mov_b64 s[44:45], 0x80
	s_mov_b32 s95, 0xc0e00000
	s_mov_b32 s46, 0xc01d265f
	v_mbcnt_hi_u32_b32 v205, -1, v0
	v_mov_b32_e32 v206, 1
	v_mov_b32_e32 v207, 0x40e00000
	v_writelane_b32 v255, s30, 42
	s_barrier
	s_branch .LBB0_1580
